# gate/up to down-projection barrier made XCD-local (no L2 write-back, no cross-XCD stage) when every workgroup sits on XCC bid&7, checked at run time
# speedup vs baseline: 1.0387x; 1.0122x over previous
_Z4mega1Pii:
	s_load_dwordx2 s[58:59], s[0:1], 0xd0
	s_mov_b64 s[60:61], s[0:1]
	s_add_u32 s0, s60, 0xe0
	s_addc_u32 s1, s61, 0
	s_mov_b32 s57, s2
	v_writelane_b32 v246, s0, 0
	v_cmp_gt_u32_e64 s[2:3], 4, v0
	s_nop 0
	v_writelane_b32 v246, s1, 1
	s_mov_b64 s[0:1], exec
	v_writelane_b32 v246, s2, 2
	s_nop 1
	v_writelane_b32 v246, s3, 3
	s_and_b64 s[2:3], s[0:1], s[2:3]
	s_mov_b64 exec, s[2:3]
	v_lshl_add_u32 v1, v0, 2, 0
	v_add_u32_e32 v1, 0x20000, v1
	v_mov_b32_e32 v2, 0
	ds_write_b32 v1, v2
	s_or_b64 exec, exec, s[0:1]
	s_load_dwordx2 s[0:1], s[60:61], 0xd8
	s_load_dword s2, s[60:61], 0xe0
	s_mov_b32 s33, 0
	v_cmp_eq_u32_e32 vcc, 0, v0
	s_mov_b32 s56, 0
	s_waitcnt lgkmcnt(0)
	v_writelane_b32 v246, s2, 4
	v_writelane_b32 v246, s0, 5
	s_barrier
	s_nop 0
	v_writelane_b32 v246, s1, 6
	s_sub_i32 s0, s1, s0
	s_cmp_lt_i32 s0, 2
	s_cbranch_scc1 .LBB0_7
	s_getreg_b32 s0, hwreg(HW_REG_XCC_ID, 0, 4)
	s_and_b32 s33, s0, 15
	s_and_saveexec_b64 s[0:1], vcc
	s_cbranch_execz .LBB0_6
	s_mov_b64 s[2:3], exec
	v_mbcnt_lo_u32_b32 v1, s2, 0
	v_mbcnt_hi_u32_b32 v1, s3, v1
	v_cmp_eq_u32_e32 vcc, 0, v1
	s_and_b64 s[4:5], exec, vcc
	s_mov_b64 exec, s[4:5]
	s_cbranch_execz .LBB0_6
	s_lshl_b32 s4, s33, 8
	s_bcnt1_i32_b64 s2, s[2:3]
	v_mov_b32_e32 v1, s4
	v_mov_b32_e32 v2, s2
	global_atomic_add v1, v2, s[58:59] offset:1024
	s_and_b32 s4, s57, 7
	s_cmp_eq_u32 s4, s33
	s_cbranch_scc1 .Lplace_ok
	v_mov_b32_e32 v1, 0
	global_atomic_add v1, v2, s[58:59] offset:32
.Lplace_ok:
.LBB0_6:
	s_or_b64 exec, exec, s[0:1]
	s_add_i32 s56, 0, 0x20000

.LBB0_1682:
	v_readlane_b32 s4, v245, 22
	v_readlane_b32 s5, v245, 23
	v_cvt_f32_u32_e32 v1, v3
	v_sub_u32_e32 v5, 0, v3
	v_rcp_iflag_f32_e32 v1, v1
	s_nop 1
	global_load_dword v19, v195, s[58:59] offset:32 sc1
	global_atomic_add v4, v195, v203, s[4:5] sc0
	v_mul_f32_e32 v1, 0x4f7ffffe, v1
	v_cvt_u32_f32_e32 v1, v1
	v_mul_lo_u32 v5, v5, v1
	v_mul_hi_u32 v5, v1, v5
	v_add_u32_e32 v1, v1, v5
	s_waitcnt vmcnt(0)
	v_mul_hi_u32 v1, v4, v1
	v_mul_lo_u32 v5, v1, v3
	v_sub_u32_e32 v5, v4, v5
	v_add_u32_e32 v6, 1, v1
	v_cmp_ge_u32_e32 vcc, v5, v3
	v_add_u32_e32 v4, 1, v4
	s_nop 0
	v_cndmask_b32_e32 v1, v1, v6, vcc
	v_sub_u32_e32 v6, v5, v3
	v_cndmask_b32_e32 v5, v5, v6, vcc
	v_add_u32_e32 v6, 1, v1
	v_cmp_ge_u32_e32 vcc, v5, v3
	s_nop 1
	v_cndmask_b32_e32 v1, v1, v6, vcc
	v_mul_lo_u32 v5, v3, v1
	v_add_u32_e32 v3, v5, v3
	v_cmp_ne_u32_e32 vcc, v4, v3
	s_and_saveexec_b64 s[4:5], vcc
	s_xor_b64 s[4:5], exec, s[4:5]
	s_cbranch_execz .LBB0_1696
	buffer_inv sc1
	v_readlane_b32 s6, v245, 24
	v_readlane_b32 s7, v245, 25
	s_waitcnt lgkmcnt(0)
	s_nop 3
	global_load_dword v2, v195, s[6:7] sc1
	s_waitcnt vmcnt(0)
	v_cmp_eq_u32_e32 vcc, v2, v1
	s_and_saveexec_b64 s[6:7], vcc
	s_cbranch_execz .LBB0_1695
	s_mov_b32 s19, 1
	s_mov_b64 s[8:9], 0
	s_branch .LBB0_1686

.LBB0_1696:
	s_andn2_saveexec_b64 s[4:5], s[4:5]
	s_cbranch_execz .LBB0_1714
	s_mov_b64 s[4:5], exec
	v_cmp_ne_u32_e32 vcc, 0, v19
	s_cbranch_vccnz .Llb_glob
	buffer_inv sc1
	v_readlane_b32 s6, v245, 24
	v_readlane_b32 s7, v245, 25
	s_nop 4
	global_atomic_add v195, v203, s[6:7]
	s_waitcnt vmcnt(0)
	s_branch .LBB0_1714
.Llb_glob:
	buffer_wbl2 sc1
	buffer_inv sc1
	s_waitcnt lgkmcnt(0)
	s_waitcnt vmcnt(0)
	v_mbcnt_lo_u32_b32 v1, s4, 0
	v_mbcnt_hi_u32_b32 v1, s5, v1
	v_cmp_eq_u32_e32 vcc, 0, v1
	s_and_saveexec_b64 s[6:7], vcc
	s_cbranch_execz .LBB0_1699
	s_bcnt1_i32_b64 s4, s[4:5]
	v_mov_b32_e32 v3, s4
	v_readlane_b32 s4, v245, 26
	v_readlane_b32 s5, v245, 27
	s_nop 4
	global_atomic_add v3, v195, v3, s[4:5] sc0
